# T10 variant: 12288 items moved, waves 1..6, one unit per wave per seam, last fill seam 14
# speedup vs baseline: 1.0065x; 1.0065x over previous
; __device__ __forceinline__ void moe_convert(Frame& F, int lo, int hi, int rank, int nrank) {
;     ...
;     for (int it = lo + rank; it < hi; it += nrank) {
;         int r = it; const float* W; unsigned char* WT; int N, ldt, kind, off; float f8s;
;         if (r < 14336) { const int e = r / 1792; r -= e * 1792; W = F.in[IN_WMG] + (size_t)e * 2048 * DFFE; N = DFFE; WT = F.ws + WS_WGU1 + (size_t)e * 14336 * 2048; ldt = 2048; kind = 1; off = 0; f8s = 32.f; }
;         else if ((r -= 14336) < 14336) { const int e = r / 1792; r -= e * 1792; W = F.in[IN_WMU] + (size_t)e * 2048 * DFFE; N = DFFE; WT = F.ws + WS_WGU1 + (size_t)e * 14336 * 2048; ldt = 2048; kind = 1; off = 128; f8s = 256.f; }
;         else { r -= 14336; const int e = r / 1792; r -= e * 1792; W = F.in[IN_WMD] + (size_t)e * DFFE * 2048; N = 2048; WT = F.ws + WS_WDN1 + (size_t)e * 2048 * DFFE; ldt = DFFE; kind = 0; off = 0; f8s = 64.f; }
.Lsf0_notw0:
	s_cmp_gt_u32 s4, 6
	s_cbranch_scc1 .Lsf0_skip
	v_mov_b32_e32 v8, 0x20020
	ds_read_b32 v9, v8 offset:4
	v_mbcnt_lo_u32_b32 v2, -1, 0
	v_mbcnt_hi_u32_b32 v2, -1, v2
	s_waitcnt lgkmcnt(0)
	v_readfirstlane_b32 s5, v9
	s_cmp_ge_u32 s5, 96
	s_cbranch_scc1 .Lsf0_skip
	s_add_i32 s5, s4, -1
	s_lshl_b32 s5, s5, 14
	v_lshl_add_u32 v7, v2, 4, s5
	ds_write_b128 v7, v[160:163] offset:0
	ds_write_b128 v7, v[164:167] offset:1024
	ds_write_b128 v7, v[168:171] offset:2048
	ds_write_b128 v7, v[172:175] offset:3072
	ds_write_b128 v7, v[176:179] offset:4096
	ds_write_b128 v7, v[180:183] offset:5120
	ds_write_b128 v7, v[184:187] offset:6144
	ds_write_b128 v7, v[188:191] offset:7168
	ds_write_b128 v7, v[192:195] offset:8192
	ds_write_b128 v7, v[196:199] offset:9216
	ds_write_b128 v7, v[200:203] offset:10240
	ds_write_b128 v7, v[204:207] offset:11264
	ds_write_b128 v7, v[208:211] offset:12288
	ds_write_b128 v7, v[212:215] offset:13312
	ds_write_b128 v7, v[216:219] offset:14336
	ds_write_b128 v7, v[220:223] offset:15360
	v_readlane_b32 s6, v247, 0
	v_readlane_b32 s7, v247, 1
	s_load_dwordx2 s[10:11], s[6:7], 0xc0
	s_load_dwordx2 s[12:13], s[6:7], 0xc8
	v_readlane_b32 s33, v247, 6
	v_mov_b32_e32 v3, 0x43e00000
	v_cmp_eq_u32_e32 vcc, 0, v2
	s_mul_i32 s33, s33, 96
	s_nop 1
	v_cndmask_b32_e64 v18, 0, 1, vcc
	s_waitcnt lgkmcnt(0)
	s_mov_b32 s34, 1

; __device__ __forceinline__ void moe_convert(Frame& F, int lo, int hi, int rank, int nrank) {
;     ...
;     for (int it = lo + rank; it < hi; it += nrank) {
;         int r = it; const float* W; unsigned char* WT; int N, ldt, kind, off; float f8s;
;         if (r < 14336) { const int e = r / 1792; r -= e * 1792; W = F.in[IN_WMG] + (size_t)e * 2048 * DFFE; N = DFFE; WT = F.ws + WS_WGU1 + (size_t)e * 14336 * 2048; ldt = 2048; kind = 1; off = 0; f8s = 32.f; }
;         else if ((r -= 14336) < 14336) { const int e = r / 1792; r -= e * 1792; W = F.in[IN_WMU] + (size_t)e * 2048 * DFFE; N = DFFE; WT = F.ws + WS_WGU1 + (size_t)e * 14336 * 2048; ldt = 2048; kind = 1; off = 128; f8s = 256.f; }
;         else { r -= 14336; const int e = r / 1792; r -= e * 1792; W = F.in[IN_WMD] + (size_t)e * DFFE * 2048; N = 2048; WT = F.ws + WS_WDN1 + (size_t)e * 2048 * DFFE; ldt = DFFE; kind = 0; off = 0; f8s = 64.f; }
.Lsf14_notw0:
	s_cmp_gt_u32 s4, 6
	s_cbranch_scc1 .Lsf14_skip
	v_mov_b32_e32 v8, 0x20020
	ds_read_b32 v9, v8 offset:4
	v_mbcnt_lo_u32_b32 v2, -1, 0
	v_mbcnt_hi_u32_b32 v2, -1, v2
	v_readlane_b32 s6, v247, 0
	v_readlane_b32 s7, v247, 1
	s_load_dword s38, s[6:7], 0xe8
	v_readlane_b32 s39, v247, 6
	s_waitcnt lgkmcnt(0)
	v_readfirstlane_b32 s5, v9
	s_mov_b32 s37, 0
	s_cmp_ge_u32 s5, 96
	s_cbranch_scc0 .Lsf14_go
	s_mov_b32 s37, 1
	s_add_i32 s5, s39, s38
	s_cmpk_ge_u32 s5, 0x100
	s_cbranch_scc1 .Lsf14_skip
.Lsf14_go:
	s_add_i32 s5, s4, -1
	s_lshl_b32 s5, s5, 14
	v_lshl_add_u32 v7, v2, 4, s5
	ds_write_b128 v7, v[160:163] offset:0
	ds_write_b128 v7, v[164:167] offset:1024
	ds_write_b128 v7, v[168:171] offset:2048
	ds_write_b128 v7, v[172:175] offset:3072
	ds_write_b128 v7, v[176:179] offset:4096
	ds_write_b128 v7, v[180:183] offset:5120
	ds_write_b128 v7, v[184:187] offset:6144
	ds_write_b128 v7, v[188:191] offset:7168
	ds_write_b128 v7, v[192:195] offset:8192
	ds_write_b128 v7, v[196:199] offset:9216
	ds_write_b128 v7, v[200:203] offset:10240
	ds_write_b128 v7, v[204:207] offset:11264
	ds_write_b128 v7, v[208:211] offset:12288
	ds_write_b128 v7, v[212:215] offset:13312
	ds_write_b128 v7, v[216:219] offset:14336
	ds_write_b128 v7, v[220:223] offset:15360
	v_readlane_b32 s6, v247, 0
	v_readlane_b32 s7, v247, 1
	s_load_dwordx2 s[10:11], s[6:7], 0xc0
	s_load_dwordx2 s[12:13], s[6:7], 0xc8
	v_readlane_b32 s33, v247, 6
	v_mov_b32_e32 v3, 0x43e00000
	v_cmp_eq_u32_e32 vcc, 0, v2
	s_mul_i32 s33, s33, 96
	s_nop 1
	v_cndmask_b32_e64 v18, 0, 1, vcc
	s_waitcnt lgkmcnt(0)
.Lsf14_loop:
	s_cmp_eq_u32 s37, 0
	s_cbranch_scc0 .Lsf14_orph
	ds_add_rtn_u32 v9, v8, v18 offset:4
	s_waitcnt lgkmcnt(0)
	v_readfirstlane_b32 s18, v9
	s_cmp_ge_u32 s18, 96
	s_cbranch_scc0 .Lsf14_own
	s_mov_b32 s37, 1
	s_branch .Lsf14_loop

; __device__ __forceinline__ void moe_convert(Frame& F, int lo, int hi, int rank, int nrank) {
;     ...
;     for (int it = lo + rank; it < hi; it += nrank) {
;         int r = it; const float* W; unsigned char* WT; int N, ldt, kind, off; float f8s;
;         if (r < 14336) { const int e = r / 1792; r -= e * 1792; W = F.in[IN_WMG] + (size_t)e * 2048 * DFFE; N = DFFE; WT = F.ws + WS_WGU1 + (size_t)e * 14336 * 2048; ldt = 2048; kind = 1; off = 0; f8s = 32.f; }
;         else if ((r -= 14336) < 14336) { const int e = r / 1792; r -= e * 1792; W = F.in[IN_WMU] + (size_t)e * 2048 * DFFE; N = DFFE; WT = F.ws + WS_WGU1 + (size_t)e * 14336 * 2048; ldt = 2048; kind = 1; off = 128; f8s = 256.f; }
;         else { r -= 14336; const int e = r / 1792; r -= e * 1792; W = F.in[IN_WMD] + (size_t)e * DFFE * 2048; N = 2048; WT = F.ws + WS_WDN1 + (size_t)e * 2048 * DFFE; ldt = DFFE; kind = 0; off = 0; f8s = 64.f; }
.Lsf14_orph:
	ds_add_rtn_u32 v9, v8, v18 offset:8
	s_waitcnt lgkmcnt(0)
	v_readfirstlane_b32 s18, v9
	s_mul_hi_u32 s35, s18, 0x2aaaaab
	s_mul_i32 s36, s35, 96
	s_sub_i32 s36, s18, s36
	s_add_i32 s35, s35, 1
	s_mul_i32 s35, s35, s38
	s_add_i32 s35, s35, s39
	s_cmpk_ge_u32 s35, 0x100
	s_cbranch_scc1 .Lsf14_done
	s_mul_i32 s35, s35, 96
	s_add_i32 s18, s35, s36
.Lsf14_unit:
	s_and_b32 s27, s18, 1
	s_lshr_b32 s19, s18, 1
	s_add_i32 s19, s19, 0x5800
	s_cmp_lt_u32 s19, 0x7000
	s_cbranch_scc0 .Lsf14_down
	s_add_i32 s20, s19, 0xffffc800
	s_lshr_b32 s21, s20, 8
	s_mul_i32 s21, s21, 37
	s_lshr_b32 s21, s21, 8
	s_mul_i32 s28, s21, 0x700
	s_sub_i32 s20, s20, s28
	s_mul_i32 s28, s21, 0x3800000
	s_add_u32 s14, s10, s28
	s_addc_u32 s15, s11, 0
	s_mul_i32 s28, s21, 0x1c00000
	s_add_u32 s28, s28, 0x7800000
	s_add_u32 s16, s86, s28
	s_addc_u32 s17, s87, 0
	s_movk_i32 s24, 0x7000
	s_movk_i32 s25, 0x800
	s_mov_b32 s26, 0x43800000
	s_lshr_b32 s22, s20, 4
	s_mul_i32 s22, s22, 0x2493
	s_lshr_b32 s22, s22, 16
	s_mul_i32 s28, s22, 0x70
	s_sub_i32 s23, s20, s28
	s_mov_b32 s29, 1
	s_branch .Lsf14_dec
